# MoE unit loops: end-of-unit store drain + barrier moved into the next unit's prologue (in front of its first LDS-DMA) so unit decode and first weight loads start earlier
# baseline (speedup 1.0000x reference)
.LBB0_1006:
	s_or_b64 exec, exec, s[36:37]
	s_nop 0
	s_add_i32 s46, s46, s80
	s_cmp_lt_i32 s46, s3
	s_nop 0
	s_nop 0
	s_cbranch_scc0 .LBB0_1025

.LBB0_1013:
	s_or_b64 exec, exec, s[34:35]
	s_lshl_b64 s[34:35], s[10:11], 22
	s_add_u32 s10, s12, s34
	s_addc_u32 s52, s13, s35
	s_lshl_b32 s34, s36, 9
	s_lshl_b32 s35, s46, 6
	s_sub_i32 s34, s35, s34
	s_ashr_i32 s35, s34, 31
	s_lshl_b64 s[36:37], s[34:35], 2
	s_add_u32 s36, s10, s36
	s_addc_u32 s37, s52, s37
	v_or_b32_e32 v146, v3, v1
	s_waitcnt lgkmcnt(0)
	v_readfirstlane_b32 s51, v2
	v_lshl_add_u64 v[2:3], s[36:37], 0, v[152:153]
	v_lshl_add_u64 v[156:157], v[2:3], 0, v[148:149]
	s_mov_b64 s[36:37], -1
	s_cmp_ge_i32 s38, s50
	v_lshl_add_u64 v[132:133], v[156:157], 0, s[22:23]
	v_lshl_add_u64 v[130:131], v[156:157], 0, s[24:25]
	v_lshl_add_u64 v[134:135], v[156:157], 0, s[26:27]
	v_lshl_add_u64 v[138:139], v[156:157], 0, s[28:29]
	v_lshl_add_u64 v[142:143], v[156:157], 0, s[30:31]
	s_cbranch_scc0 .LBB0_1017
	global_load_dwordx4 v[2:5], v[156:157], off sc1 nt
	s_mov_b32 m0, s39
	global_load_dwordx4 v[6:9], v[132:133], off sc1 nt
	v_lshl_add_u64 v[50:51], s[14:15], 0, v[146:147]
	s_waitcnt lgkmcnt(0)
	s_barrier
	global_load_lds_dwordx4 v146, s[14:15]
	global_load_dwordx4 v[34:37], v[130:131], off sc1 nt
	global_load_dwordx4 v[38:41], v[134:135], off sc1 nt
	s_mov_b32 m0, s40
	s_nop 0
	global_load_lds_dwordx4 v146, s[16:17]
	s_waitcnt vmcnt(4)
	s_nop 0
	v_cvt_pk_bf16_f32 v2, v2, v6
	ds_write_b32 v169, v2 offset:49152
	v_cvt_pk_bf16_f32 v2, v3, v7
	ds_write_b32 v169, v2 offset:49216
	v_cvt_pk_bf16_f32 v2, v4, v8
	ds_write_b32 v169, v2 offset:49280
	v_cvt_pk_bf16_f32 v2, v5, v9
	ds_write_b32 v169, v2 offset:49344
	global_load_dwordx4 v[42:45], v[138:139], off sc1 nt
	global_load_dwordx4 v[46:49], v[142:143], off sc1 nt
	s_waitcnt vmcnt(5)
	s_mov_b32 m0, s41
	s_waitcnt lgkmcnt(0)
	s_barrier
	global_load_lds_dwordx4 v146, s[18:19]
	v_mov_b32_e32 v2, 0
	s_mov_b32 s37, -2
	s_movk_i32 s36, 0x80
	v_mov_b32_e32 v3, v2
	v_mov_b32_e32 v4, v2
	v_mov_b32_e32 v5, v2
	v_mov_b32_e32 v6, v2
	v_mov_b32_e32 v7, v2
	v_mov_b32_e32 v8, v2
	v_mov_b32_e32 v9, v2
	v_mov_b32_e32 v10, v2
	v_mov_b32_e32 v11, v2
	v_mov_b32_e32 v12, v2
	v_mov_b32_e32 v13, v2
	v_mov_b32_e32 v14, v2
	v_mov_b32_e32 v15, v2
	v_mov_b32_e32 v16, v2
	v_mov_b32_e32 v17, v2
	v_mov_b32_e32 v66, v2
	v_mov_b32_e32 v67, v2
	v_mov_b32_e32 v68, v2
	v_mov_b32_e32 v69, v2
	v_mov_b32_e32 v70, v2
	v_mov_b32_e32 v71, v2
	v_mov_b32_e32 v72, v2
	v_mov_b32_e32 v73, v2
	v_mov_b32_e32 v74, v2
	v_mov_b32_e32 v75, v2
	v_mov_b32_e32 v76, v2
	v_mov_b32_e32 v77, v2
	v_mov_b32_e32 v78, v2
	v_mov_b32_e32 v79, v2
	v_mov_b32_e32 v80, v2
	v_mov_b32_e32 v81, v2
	v_mov_b32_e32 v18, v2
	v_mov_b32_e32 v19, v2
	v_mov_b32_e32 v20, v2
	v_mov_b32_e32 v21, v2
	v_mov_b32_e32 v22, v2
	v_mov_b32_e32 v23, v2
	v_mov_b32_e32 v24, v2
	v_mov_b32_e32 v25, v2
	v_mov_b32_e32 v26, v2
	v_mov_b32_e32 v27, v2
	v_mov_b32_e32 v28, v2
	v_mov_b32_e32 v29, v2
	v_mov_b32_e32 v30, v2
	v_mov_b32_e32 v31, v2
	v_mov_b32_e32 v32, v2
	v_mov_b32_e32 v33, v2
	v_mov_b32_e32 v114, v2
	v_mov_b32_e32 v115, v2
	v_mov_b32_e32 v116, v2
	v_mov_b32_e32 v117, v2
	v_mov_b32_e32 v118, v2
	v_mov_b32_e32 v119, v2
	v_mov_b32_e32 v120, v2
	v_mov_b32_e32 v121, v2
	v_mov_b32_e32 v122, v2
	v_mov_b32_e32 v123, v2
	v_mov_b32_e32 v124, v2
	v_mov_b32_e32 v125, v2
	v_mov_b32_e32 v126, v2
	v_mov_b32_e32 v127, v2
	v_mov_b32_e32 v128, v2
	v_mov_b32_e32 v129, v2
	v_readfirstlane_b32 s98, v250
	s_bitcmp1_b32 s98, 6
	s_cbranch_scc1 .Lmoe_B_1015

.LBB0_1017:
	v_mov_b32_e32 v97, 0
	s_and_b64 vcc, exec, s[36:37]
	v_mov_b32_e32 v96, v97
	v_mov_b32_e32 v95, v97
	v_mov_b32_e32 v94, v97
	v_mov_b32_e32 v93, v97
	v_mov_b32_e32 v92, v97
	v_mov_b32_e32 v91, v97
	v_mov_b32_e32 v90, v97
	v_mov_b32_e32 v89, v97
	v_mov_b32_e32 v88, v97
	v_mov_b32_e32 v87, v97
	v_mov_b32_e32 v86, v97
	v_mov_b32_e32 v85, v97
	v_mov_b32_e32 v84, v97
	v_mov_b32_e32 v83, v97
	v_mov_b32_e32 v82, v97
	v_mov_b32_e32 v65, v97
	v_mov_b32_e32 v64, v97
	v_mov_b32_e32 v63, v97
	v_mov_b32_e32 v62, v97
	v_mov_b32_e32 v61, v97
	v_mov_b32_e32 v60, v97
	v_mov_b32_e32 v59, v97
	v_mov_b32_e32 v58, v97
	v_mov_b32_e32 v57, v97
	v_mov_b32_e32 v56, v97
	v_mov_b32_e32 v55, v97
	v_mov_b32_e32 v54, v97
	v_mov_b32_e32 v53, v97
	v_mov_b32_e32 v52, v97
	v_mov_b32_e32 v51, v97
	v_mov_b32_e32 v50, v97
	v_mov_b32_e32 v113, v97
	v_mov_b32_e32 v112, v97
	v_mov_b32_e32 v111, v97
	v_mov_b32_e32 v110, v97
	v_mov_b32_e32 v109, v97
	v_mov_b32_e32 v108, v97
	v_mov_b32_e32 v107, v97
	v_mov_b32_e32 v106, v97
	v_mov_b32_e32 v105, v97
	v_mov_b32_e32 v104, v97
	v_mov_b32_e32 v103, v97
	v_mov_b32_e32 v102, v97
	v_mov_b32_e32 v101, v97
	v_mov_b32_e32 v100, v97
	v_mov_b32_e32 v99, v97
	v_mov_b32_e32 v98, v97
	v_mov_b32_e32 v49, v97
	v_mov_b32_e32 v48, v97
	v_mov_b32_e32 v47, v97
	v_mov_b32_e32 v46, v97
	v_mov_b32_e32 v45, v97
	v_mov_b32_e32 v44, v97
	v_mov_b32_e32 v43, v97
	v_mov_b32_e32 v42, v97
	v_mov_b32_e32 v41, v97
	v_mov_b32_e32 v40, v97
	v_mov_b32_e32 v39, v97
	v_mov_b32_e32 v38, v97
	v_mov_b32_e32 v37, v97
	v_mov_b32_e32 v36, v97
	v_mov_b32_e32 v35, v97
	v_mov_b32_e32 v34, v97
	s_cbranch_vccz .LBB0_1021
	global_load_dwordx4 v[2:5], v[156:157], off sc1 nt
	s_mov_b32 m0, s39
	global_load_dwordx4 v[6:9], v[132:133], off sc1 nt
	v_or_b32_e32 v158, v136, v1
	s_waitcnt lgkmcnt(0)
	s_barrier
	global_load_lds_dwordx4 v146, s[14:15]
	s_mov_b32 m0, s42
	v_mov_b32_e32 v159, v147
	global_load_lds_dwordx4 v158, s[14:15]
	global_load_dwordx4 v[130:133], v[130:131], off sc1 nt
	global_load_dwordx4 v[134:137], v[134:135], off sc1 nt
	s_mov_b32 m0, s40
	s_nop 0
	global_load_lds_dwordx4 v146, s[16:17]
	s_mov_b32 m0, s43
	s_nop 0
	global_load_lds_dwordx4 v158, s[16:17]
	s_waitcnt vmcnt(6)
	s_nop 0
	v_cvt_pk_bf16_f32 v2, v2, v6
	ds_write_b32 v169, v2 offset:49152
	v_cvt_pk_bf16_f32 v2, v3, v7
	ds_write_b32 v169, v2 offset:49216
	v_cvt_pk_bf16_f32 v2, v4, v8
	ds_write_b32 v169, v2 offset:49280
	v_cvt_pk_bf16_f32 v2, v5, v9
	ds_write_b32 v169, v2 offset:49344
	global_load_dwordx4 v[138:141], v[138:139], off sc1 nt
	global_load_dwordx4 v[142:145], v[142:143], off sc1 nt
	s_waitcnt vmcnt(6)
	s_mov_b32 m0, s41
	s_waitcnt lgkmcnt(0)
	s_barrier
	global_load_lds_dwordx4 v146, s[18:19]
	s_mov_b32 m0, s44
	v_mov_b32_e32 v34, 0
	global_load_lds_dwordx4 v158, s[18:19]
	s_mov_b32 s37, -2
	s_movk_i32 s36, 0x80
	v_mov_b32_e32 v35, v34
	v_mov_b32_e32 v36, v34
	v_mov_b32_e32 v37, v34
	v_mov_b32_e32 v38, v34
	v_mov_b32_e32 v39, v34
	v_mov_b32_e32 v40, v34
	v_mov_b32_e32 v41, v34
	v_mov_b32_e32 v42, v34
	v_mov_b32_e32 v43, v34
	v_mov_b32_e32 v44, v34
	v_mov_b32_e32 v45, v34
	v_mov_b32_e32 v46, v34
	v_mov_b32_e32 v47, v34
	v_mov_b32_e32 v48, v34
	v_mov_b32_e32 v49, v34
	v_mov_b32_e32 v98, v34
	v_mov_b32_e32 v99, v34
	v_mov_b32_e32 v100, v34
	v_mov_b32_e32 v101, v34
	v_mov_b32_e32 v102, v34
	v_mov_b32_e32 v103, v34
	v_mov_b32_e32 v104, v34
	v_mov_b32_e32 v105, v34
	v_mov_b32_e32 v106, v34
	v_mov_b32_e32 v107, v34
	v_mov_b32_e32 v108, v34
	v_mov_b32_e32 v109, v34
	v_mov_b32_e32 v110, v34
	v_mov_b32_e32 v111, v34
	v_mov_b32_e32 v112, v34
	v_mov_b32_e32 v113, v34
	v_mov_b32_e32 v50, v34
	v_mov_b32_e32 v51, v34
	v_mov_b32_e32 v52, v34
	v_mov_b32_e32 v53, v34
	v_mov_b32_e32 v54, v34
	v_mov_b32_e32 v55, v34
	v_mov_b32_e32 v56, v34
	v_mov_b32_e32 v57, v34
	v_mov_b32_e32 v58, v34
	v_mov_b32_e32 v59, v34
	v_mov_b32_e32 v60, v34
	v_mov_b32_e32 v61, v34
	v_mov_b32_e32 v62, v34
	v_mov_b32_e32 v63, v34
	v_mov_b32_e32 v64, v34
	v_mov_b32_e32 v65, v34
	v_mov_b32_e32 v82, v34
	v_mov_b32_e32 v83, v34
	v_mov_b32_e32 v84, v34
	v_mov_b32_e32 v85, v34
	v_mov_b32_e32 v86, v34
	v_mov_b32_e32 v87, v34
	v_mov_b32_e32 v88, v34
	v_mov_b32_e32 v89, v34
	v_mov_b32_e32 v90, v34
	v_mov_b32_e32 v91, v34
	v_mov_b32_e32 v92, v34
	v_mov_b32_e32 v93, v34
	v_mov_b32_e32 v94, v34
	v_mov_b32_e32 v95, v34
	v_mov_b32_e32 v96, v34
	v_mov_b32_e32 v97, v34
	v_mov_b32_e32 v2, v34
	v_mov_b32_e32 v3, v34
	v_mov_b32_e32 v4, v34
	v_mov_b32_e32 v5, v34
	v_mov_b32_e32 v6, v34
	v_mov_b32_e32 v7, v34
	v_mov_b32_e32 v8, v34
	v_mov_b32_e32 v9, v34
	v_mov_b32_e32 v10, v34
	v_mov_b32_e32 v11, v34
	v_mov_b32_e32 v12, v34
	v_mov_b32_e32 v13, v34
	v_mov_b32_e32 v14, v34
	v_mov_b32_e32 v15, v34
	v_mov_b32_e32 v16, v34
	v_mov_b32_e32 v17, v34
	v_mov_b32_e32 v66, v34
	v_mov_b32_e32 v67, v34
	v_mov_b32_e32 v68, v34
	v_mov_b32_e32 v69, v34
	v_mov_b32_e32 v70, v34
	v_mov_b32_e32 v71, v34
	v_mov_b32_e32 v72, v34
	v_mov_b32_e32 v73, v34
	v_mov_b32_e32 v74, v34
	v_mov_b32_e32 v75, v34
	v_mov_b32_e32 v76, v34
	v_mov_b32_e32 v77, v34
	v_mov_b32_e32 v78, v34
	v_mov_b32_e32 v79, v34
	v_mov_b32_e32 v80, v34
	v_mov_b32_e32 v81, v34
	v_mov_b32_e32 v18, v34
	v_mov_b32_e32 v19, v34
	v_mov_b32_e32 v20, v34
	v_mov_b32_e32 v21, v34
	v_mov_b32_e32 v22, v34
	v_mov_b32_e32 v23, v34
	v_mov_b32_e32 v24, v34
	v_mov_b32_e32 v25, v34
	v_mov_b32_e32 v26, v34
	v_mov_b32_e32 v27, v34
	v_mov_b32_e32 v28, v34
	v_mov_b32_e32 v29, v34
	v_mov_b32_e32 v30, v34
	v_mov_b32_e32 v31, v34
	v_mov_b32_e32 v32, v34
	v_mov_b32_e32 v33, v34
	v_mov_b32_e32 v114, v34
	v_mov_b32_e32 v115, v34
	v_mov_b32_e32 v116, v34
	v_mov_b32_e32 v117, v34
	v_mov_b32_e32 v118, v34
	v_mov_b32_e32 v119, v34
	v_mov_b32_e32 v120, v34
	v_mov_b32_e32 v121, v34
	v_mov_b32_e32 v122, v34
	v_mov_b32_e32 v123, v34
	v_mov_b32_e32 v124, v34
	v_mov_b32_e32 v125, v34
	v_mov_b32_e32 v126, v34
	v_mov_b32_e32 v127, v34
	v_mov_b32_e32 v128, v34
	v_mov_b32_e32 v129, v34
	v_readfirstlane_b32 s98, v250
	s_bitcmp1_b32 s98, 6
	s_cbranch_scc1 .Lmoe_B_1019

.LBB0_1082:
	s_or_b64 exec, exec, s[34:35]
	s_nop 0
	s_add_i32 s46, s46, s80
	s_cmp_lt_i32 s46, s3
	s_nop 0
	s_nop 0
	s_cbranch_scc0 .LBB0_1097

.LBB0_1084:
	s_add_i32 s31, s30, s34
	s_lshl_b32 s35, s31, 2
	s_add_i32 s35, s35, 0
	s_add_i32 s35, s35, 0x20000
	v_mov_b32_e32 v2, s35
	ds_read_b32 v2, v2
	s_waitcnt lgkmcnt(0)
	v_readfirstlane_b32 s35, v2
	s_cmp_gt_i32 s35, s10
	s_cselect_b32 s34, s34, s31
	s_lshr_b32 s31, s30, 1
	s_cmp_lt_u32 s30, 2
	s_mov_b32 s30, s31
	s_cbranch_scc0 .LBB0_1084
	s_lshl_b32 s30, s34, 2
	s_add_i32 s30, s30, 0
	s_add_i32 s30, s30, 0x20000
	v_mov_b32_e32 v4, s30
	ds_read2_b32 v[2:3], v4 offset1:80
	ds_read_b32 v4, v4 offset:640
	s_mov_b32 s35, s11
	s_waitcnt lgkmcnt(1)
	v_readfirstlane_b32 s30, v2
	s_sub_i32 s30, s10, s30
	v_readfirstlane_b32 s31, v3
	s_lshl_b32 s47, s30, 9
	s_waitcnt lgkmcnt(0)
	v_readfirstlane_b32 s49, v4
	s_sub_i32 s30, s31, s47
	s_add_i32 s49, s49, s47
	s_min_i32 s48, s30, 0x200
	s_lshl_b64 s[30:31], s[34:35], 22
	s_add_u32 s35, s6, s30
	s_addc_u32 s50, s7, s31
	s_lshl_b32 s10, s10, 11
	s_lshl_b32 s30, s46, 7
	s_sub_i32 s30, s30, s10
	s_ashr_i32 s31, s30, 31
	v_cmp_gt_i32_e32 vcc, s48, v0
	s_lshl_b64 s[36:37], s[30:31], 2
	s_add_u32 s36, s35, s36
	v_cndmask_b32_e32 v2, 0, v0, vcc
	v_add_u32_e32 v2, s49, v2
	s_addc_u32 s37, s50, s37
	v_lshl_or_b32 v146, v2, 9, v1
	v_lshl_add_u64 v[2:3], s[36:37], 0, v[152:153]
	v_lshl_add_u64 v[154:155], v[2:3], 0, v[148:149]
	s_mov_b64 s[36:37], -1
	s_cmp_ge_i32 s38, s48
	v_lshl_add_u64 v[132:133], v[154:155], 0, s[20:21]
	v_lshl_add_u64 v[130:131], v[154:155], 0, s[22:23]
	v_lshl_add_u64 v[134:135], v[154:155], 0, s[24:25]
	v_lshl_add_u64 v[138:139], v[154:155], 0, s[26:27]
	v_lshl_add_u64 v[142:143], v[154:155], 0, s[28:29]
	s_cbranch_scc0 .LBB0_1089
	global_load_dwordx4 v[2:5], v[154:155], off sc1 nt
	s_mov_b32 m0, s39
	global_load_dwordx4 v[6:9], v[132:133], off sc1 nt
	v_lshl_add_u64 v[82:83], s[12:13], 0, v[146:147]
	s_waitcnt lgkmcnt(0)
	s_barrier
	global_load_lds_dwordx4 v146, s[12:13]
	global_load_dwordx4 v[66:69], v[130:131], off sc1 nt
	global_load_dwordx4 v[70:73], v[134:135], off sc1 nt
	s_mov_b32 m0, s40
	s_nop 0
	global_load_lds_dwordx4 v146, s[14:15]
	s_waitcnt vmcnt(4)
	s_nop 0
	v_cvt_pk_bf16_f32 v2, v2, v6
	ds_write_b32 v167, v2 offset:49152
	v_cvt_pk_bf16_f32 v2, v3, v7
	ds_write_b32 v167, v2 offset:49216
	v_cvt_pk_bf16_f32 v2, v4, v8
	ds_write_b32 v167, v2 offset:49280
	v_cvt_pk_bf16_f32 v2, v5, v9
	ds_write_b32 v167, v2 offset:49344
	global_load_dwordx4 v[74:77], v[138:139], off sc1 nt
	global_load_dwordx4 v[78:81], v[142:143], off sc1 nt
	s_waitcnt vmcnt(5)
	s_mov_b32 m0, s41
	s_waitcnt lgkmcnt(0)
	s_barrier
	global_load_lds_dwordx4 v146, s[16:17]
	v_mov_b32_e32 v2, 0
	s_mov_b32 s36, -2
	s_movk_i32 s35, 0x80
	v_mov_b32_e32 v3, v2
	v_mov_b32_e32 v4, v2
	v_mov_b32_e32 v5, v2
	v_mov_b32_e32 v6, v2
	v_mov_b32_e32 v7, v2
	v_mov_b32_e32 v8, v2
	v_mov_b32_e32 v9, v2
	v_mov_b32_e32 v10, v2
	v_mov_b32_e32 v11, v2
	v_mov_b32_e32 v12, v2
	v_mov_b32_e32 v13, v2
	v_mov_b32_e32 v14, v2
	v_mov_b32_e32 v15, v2
	v_mov_b32_e32 v16, v2
	v_mov_b32_e32 v17, v2
	v_mov_b32_e32 v18, v2
	v_mov_b32_e32 v19, v2
	v_mov_b32_e32 v20, v2
	v_mov_b32_e32 v21, v2
	v_mov_b32_e32 v22, v2
	v_mov_b32_e32 v23, v2
	v_mov_b32_e32 v24, v2
	v_mov_b32_e32 v25, v2
	v_mov_b32_e32 v26, v2
	v_mov_b32_e32 v27, v2
	v_mov_b32_e32 v28, v2
	v_mov_b32_e32 v29, v2
	v_mov_b32_e32 v30, v2
	v_mov_b32_e32 v31, v2
	v_mov_b32_e32 v32, v2
	v_mov_b32_e32 v33, v2
	v_mov_b32_e32 v34, v2
	v_mov_b32_e32 v35, v2
	v_mov_b32_e32 v36, v2
	v_mov_b32_e32 v37, v2
	v_mov_b32_e32 v38, v2
	v_mov_b32_e32 v39, v2
	v_mov_b32_e32 v40, v2
	v_mov_b32_e32 v41, v2
	v_mov_b32_e32 v42, v2
	v_mov_b32_e32 v43, v2
	v_mov_b32_e32 v44, v2
	v_mov_b32_e32 v45, v2
	v_mov_b32_e32 v46, v2
	v_mov_b32_e32 v47, v2
	v_mov_b32_e32 v48, v2
	v_mov_b32_e32 v49, v2
	v_mov_b32_e32 v50, v2
	v_mov_b32_e32 v51, v2
	v_mov_b32_e32 v52, v2
	v_mov_b32_e32 v53, v2
	v_mov_b32_e32 v54, v2
	v_mov_b32_e32 v55, v2
	v_mov_b32_e32 v56, v2
	v_mov_b32_e32 v57, v2
	v_mov_b32_e32 v58, v2
	v_mov_b32_e32 v59, v2
	v_mov_b32_e32 v60, v2
	v_mov_b32_e32 v61, v2
	v_mov_b32_e32 v62, v2
	v_mov_b32_e32 v63, v2
	v_mov_b32_e32 v64, v2
	v_mov_b32_e32 v65, v2
	v_readfirstlane_b32 s98, v250
	s_bitcmp1_b32 s98, 6
	s_cbranch_scc1 .Lmoe_B_1087

.LBB0_1089:
	v_mov_b32_e32 v129, 0
	s_and_b64 vcc, exec, s[36:37]
	v_mov_b32_e32 v128, v129
	v_mov_b32_e32 v127, v129
	v_mov_b32_e32 v126, v129
	v_mov_b32_e32 v125, v129
	v_mov_b32_e32 v124, v129
	v_mov_b32_e32 v123, v129
	v_mov_b32_e32 v122, v129
	v_mov_b32_e32 v121, v129
	v_mov_b32_e32 v120, v129
	v_mov_b32_e32 v119, v129
	v_mov_b32_e32 v118, v129
	v_mov_b32_e32 v117, v129
	v_mov_b32_e32 v116, v129
	v_mov_b32_e32 v115, v129
	v_mov_b32_e32 v114, v129
	v_mov_b32_e32 v113, v129
	v_mov_b32_e32 v112, v129
	v_mov_b32_e32 v111, v129
	v_mov_b32_e32 v110, v129
	v_mov_b32_e32 v109, v129
	v_mov_b32_e32 v108, v129
	v_mov_b32_e32 v107, v129
	v_mov_b32_e32 v106, v129
	v_mov_b32_e32 v105, v129
	v_mov_b32_e32 v104, v129
	v_mov_b32_e32 v103, v129
	v_mov_b32_e32 v102, v129
	v_mov_b32_e32 v101, v129
	v_mov_b32_e32 v100, v129
	v_mov_b32_e32 v99, v129
	v_mov_b32_e32 v98, v129
	v_mov_b32_e32 v97, v129
	v_mov_b32_e32 v96, v129
	v_mov_b32_e32 v95, v129
	v_mov_b32_e32 v94, v129
	v_mov_b32_e32 v93, v129
	v_mov_b32_e32 v92, v129
	v_mov_b32_e32 v91, v129
	v_mov_b32_e32 v90, v129
	v_mov_b32_e32 v89, v129
	v_mov_b32_e32 v88, v129
	v_mov_b32_e32 v87, v129
	v_mov_b32_e32 v86, v129
	v_mov_b32_e32 v85, v129
	v_mov_b32_e32 v84, v129
	v_mov_b32_e32 v83, v129
	v_mov_b32_e32 v82, v129
	v_mov_b32_e32 v81, v129
	v_mov_b32_e32 v80, v129
	v_mov_b32_e32 v79, v129
	v_mov_b32_e32 v78, v129
	v_mov_b32_e32 v77, v129
	v_mov_b32_e32 v76, v129
	v_mov_b32_e32 v75, v129
	v_mov_b32_e32 v74, v129
	v_mov_b32_e32 v73, v129
	v_mov_b32_e32 v72, v129
	v_mov_b32_e32 v71, v129
	v_mov_b32_e32 v70, v129
	v_mov_b32_e32 v69, v129
	v_mov_b32_e32 v68, v129
	v_mov_b32_e32 v67, v129
	v_mov_b32_e32 v66, v129
	s_cbranch_vccz .LBB0_1093
	v_cmp_gt_i32_e32 vcc, s48, v165
	s_mov_b32 m0, s39
	v_mov_b32_e32 v157, v147
	v_cndmask_b32_e32 v2, 0, v165, vcc
	v_add_u32_e32 v2, s49, v2
	v_lshl_or_b32 v156, v2, 9, v1
	global_load_dwordx4 v[2:5], v[154:155], off sc1 nt
	global_load_dwordx4 v[6:9], v[132:133], off sc1 nt
	s_waitcnt lgkmcnt(0)
	s_barrier
	global_load_lds_dwordx4 v146, s[12:13]
	s_mov_b32 m0, s42
	s_nop 0
	global_load_lds_dwordx4 v156, s[12:13]
	global_load_dwordx4 v[130:133], v[130:131], off sc1 nt
	global_load_dwordx4 v[134:137], v[134:135], off sc1 nt
	s_mov_b32 m0, s40
	s_nop 0
	global_load_lds_dwordx4 v146, s[14:15]
	s_mov_b32 m0, s43
	s_nop 0
	global_load_lds_dwordx4 v156, s[14:15]
	s_waitcnt vmcnt(6)
	s_nop 0
	v_cvt_pk_bf16_f32 v2, v2, v6
	ds_write_b32 v167, v2 offset:49152
	v_cvt_pk_bf16_f32 v2, v3, v7
	ds_write_b32 v167, v2 offset:49216
	v_cvt_pk_bf16_f32 v2, v4, v8
	ds_write_b32 v167, v2 offset:49280
	v_cvt_pk_bf16_f32 v2, v5, v9
	ds_write_b32 v167, v2 offset:49344
	global_load_dwordx4 v[138:141], v[138:139], off sc1 nt
	global_load_dwordx4 v[142:145], v[142:143], off sc1 nt
	s_waitcnt vmcnt(6)
	s_mov_b32 m0, s41
	s_waitcnt lgkmcnt(0)
	s_barrier
	global_load_lds_dwordx4 v146, s[16:17]
	s_mov_b32 m0, s44
	v_mov_b32_e32 v66, 0
	global_load_lds_dwordx4 v156, s[16:17]
	s_mov_b32 s36, -2
	s_movk_i32 s35, 0x80
	v_mov_b32_e32 v67, v66
	v_mov_b32_e32 v68, v66
	v_mov_b32_e32 v69, v66
	v_mov_b32_e32 v70, v66
	v_mov_b32_e32 v71, v66
	v_mov_b32_e32 v72, v66
	v_mov_b32_e32 v73, v66
	v_mov_b32_e32 v74, v66
	v_mov_b32_e32 v75, v66
	v_mov_b32_e32 v76, v66
	v_mov_b32_e32 v77, v66
	v_mov_b32_e32 v78, v66
	v_mov_b32_e32 v79, v66
	v_mov_b32_e32 v80, v66
	v_mov_b32_e32 v81, v66
	v_mov_b32_e32 v82, v66
	v_mov_b32_e32 v83, v66
	v_mov_b32_e32 v84, v66
	v_mov_b32_e32 v85, v66
	v_mov_b32_e32 v86, v66
	v_mov_b32_e32 v87, v66
	v_mov_b32_e32 v88, v66
	v_mov_b32_e32 v89, v66
	v_mov_b32_e32 v90, v66
	v_mov_b32_e32 v91, v66
	v_mov_b32_e32 v92, v66
	v_mov_b32_e32 v93, v66
	v_mov_b32_e32 v94, v66
	v_mov_b32_e32 v95, v66
	v_mov_b32_e32 v96, v66
	v_mov_b32_e32 v97, v66
	v_mov_b32_e32 v98, v66
	v_mov_b32_e32 v99, v66
	v_mov_b32_e32 v100, v66
	v_mov_b32_e32 v101, v66
	v_mov_b32_e32 v102, v66
	v_mov_b32_e32 v103, v66
	v_mov_b32_e32 v104, v66
	v_mov_b32_e32 v105, v66
	v_mov_b32_e32 v106, v66
	v_mov_b32_e32 v107, v66
	v_mov_b32_e32 v108, v66
	v_mov_b32_e32 v109, v66
	v_mov_b32_e32 v110, v66
	v_mov_b32_e32 v111, v66
	v_mov_b32_e32 v112, v66
	v_mov_b32_e32 v113, v66
	v_mov_b32_e32 v114, v66
	v_mov_b32_e32 v115, v66
	v_mov_b32_e32 v116, v66
	v_mov_b32_e32 v117, v66
	v_mov_b32_e32 v118, v66
	v_mov_b32_e32 v119, v66
	v_mov_b32_e32 v120, v66
	v_mov_b32_e32 v121, v66
	v_mov_b32_e32 v122, v66
	v_mov_b32_e32 v123, v66
	v_mov_b32_e32 v124, v66
	v_mov_b32_e32 v125, v66
	v_mov_b32_e32 v126, v66
	v_mov_b32_e32 v127, v66
	v_mov_b32_e32 v128, v66
	v_mov_b32_e32 v129, v66
	v_mov_b32_e32 v2, v66
	v_mov_b32_e32 v3, v66
	v_mov_b32_e32 v4, v66
	v_mov_b32_e32 v5, v66
	v_mov_b32_e32 v6, v66
	v_mov_b32_e32 v7, v66
	v_mov_b32_e32 v8, v66
	v_mov_b32_e32 v9, v66
	v_mov_b32_e32 v10, v66
	v_mov_b32_e32 v11, v66
	v_mov_b32_e32 v12, v66
	v_mov_b32_e32 v13, v66
	v_mov_b32_e32 v14, v66
	v_mov_b32_e32 v15, v66
	v_mov_b32_e32 v16, v66
	v_mov_b32_e32 v17, v66
	v_mov_b32_e32 v18, v66
	v_mov_b32_e32 v19, v66
	v_mov_b32_e32 v20, v66
	v_mov_b32_e32 v21, v66
	v_mov_b32_e32 v22, v66
	v_mov_b32_e32 v23, v66
	v_mov_b32_e32 v24, v66
	v_mov_b32_e32 v25, v66
	v_mov_b32_e32 v26, v66
	v_mov_b32_e32 v27, v66
	v_mov_b32_e32 v28, v66
	v_mov_b32_e32 v29, v66
	v_mov_b32_e32 v30, v66
	v_mov_b32_e32 v31, v66
	v_mov_b32_e32 v32, v66
	v_mov_b32_e32 v33, v66
	v_mov_b32_e32 v34, v66
	v_mov_b32_e32 v35, v66
	v_mov_b32_e32 v36, v66
	v_mov_b32_e32 v37, v66
	v_mov_b32_e32 v38, v66
	v_mov_b32_e32 v39, v66
	v_mov_b32_e32 v40, v66
	v_mov_b32_e32 v41, v66
	v_mov_b32_e32 v42, v66
	v_mov_b32_e32 v43, v66
	v_mov_b32_e32 v44, v66
	v_mov_b32_e32 v45, v66
	v_mov_b32_e32 v46, v66
	v_mov_b32_e32 v47, v66
	v_mov_b32_e32 v48, v66
	v_mov_b32_e32 v49, v66
	v_mov_b32_e32 v50, v66
	v_mov_b32_e32 v51, v66
	v_mov_b32_e32 v52, v66
	v_mov_b32_e32 v53, v66
	v_mov_b32_e32 v54, v66
	v_mov_b32_e32 v55, v66
	v_mov_b32_e32 v56, v66
	v_mov_b32_e32 v57, v66
	v_mov_b32_e32 v58, v66
	v_mov_b32_e32 v59, v66
	v_mov_b32_e32 v60, v66
	v_mov_b32_e32 v61, v66
	v_mov_b32_e32 v62, v66
	v_mov_b32_e32 v63, v66
	v_mov_b32_e32 v64, v66
	v_mov_b32_e32 v65, v66
	v_readfirstlane_b32 s98, v250
	s_bitcmp1_b32 s98, 6
	s_cbranch_scc1 .Lmoe_B_1091
